# v18 + LayerNorm-1 phase: the two LDS staging loops (router weights, per-batch adaLN vectors) issue all their loads before waiting instead of one load per trip behind vmcnt(0)
# speedup vs baseline: 1.0243x; 1.0037x over previous
.LBB0_770:
	s_cmp_lt_i32 s90, 8
	s_cselect_b64 s[2:3], -1, 0
	s_and_b64 s[2:3], s[2:3], s[0:1]
	s_andn2_b64 vcc, exec, s[2:3]
	s_cbranch_vccnz .LBB0_783
	v_and_b32_e32 v1, 0x1fc, v0
	s_waitcnt vmcnt(0) lgkmcnt(0)
	v_add_u32_e32 v4, 0, v1
	v_or_b32_e32 v1, 0xfffffe00, v0
	v_lshlrev_b32_e32 v2, 4, v0
	v_mov_b32_e32 v3, 0
	v_lshlrev_b32_e32 v102, 2, v0
	v_lshl_add_u64 v[2:3], s[50:51], 0, v[2:3]
	s_mov_b64 s[0:1], 0
	s_movk_i32 s6, 0x2010
	s_mov_b64 s[4:5], 0x2000
	s_movk_i32 s7, 0x1dff
	v_mov_b32_e32 v5, v102
	v_mov_b32_e32 v6, v1
	global_load_dwordx4 v[164:167], v[2:3], off
	v_lshl_add_u64 v[2:3], v[2:3], 0, s[4:5]
	global_load_dwordx4 v[168:171], v[2:3], off
	v_lshl_add_u64 v[2:3], v[2:3], 0, s[4:5]
	global_load_dwordx4 v[172:175], v[2:3], off
	v_lshl_add_u64 v[2:3], v[2:3], 0, s[4:5]
	global_load_dwordx4 v[176:179], v[2:3], off
	v_lshl_add_u64 v[2:3], v[2:3], 0, s[4:5]
	global_load_dwordx4 v[180:183], v[2:3], off
	v_lshl_add_u64 v[2:3], v[2:3], 0, s[4:5]
	global_load_dwordx4 v[184:187], v[2:3], off
	v_lshl_add_u64 v[2:3], v[2:3], 0, s[4:5]
	global_load_dwordx4 v[188:191], v[2:3], off
	v_lshl_add_u64 v[2:3], v[2:3], 0, s[4:5]
	global_load_dwordx4 v[192:195], v[2:3], off
	v_lshl_add_u64 v[2:3], v[2:3], 0, s[4:5]
	global_load_dwordx4 v[200:203], v[2:3], off
	v_lshl_add_u64 v[2:3], v[2:3], 0, s[4:5]
	global_load_dwordx4 v[204:207], v[2:3], off
	v_lshl_add_u64 v[2:3], v[2:3], 0, s[4:5]
	global_load_dwordx4 v[208:211], v[2:3], off
	v_lshl_add_u64 v[2:3], v[2:3], 0, s[4:5]
	global_load_dwordx4 v[212:215], v[2:3], off
	v_lshl_add_u64 v[2:3], v[2:3], 0, s[4:5]
	global_load_dwordx4 v[216:219], v[2:3], off
	v_lshl_add_u64 v[2:3], v[2:3], 0, s[4:5]
	global_load_dwordx4 v[220:223], v[2:3], off
	v_lshl_add_u64 v[2:3], v[2:3], 0, s[4:5]
	global_load_dwordx4 v[224:227], v[2:3], off
	v_lshl_add_u64 v[2:3], v[2:3], 0, s[4:5]
	global_load_dwordx4 v[228:231], v[2:3], off
	v_lshl_add_u64 v[2:3], v[2:3], 0, s[4:5]
	v_and_b32_e32 v7, 12, v5
	v_mad_u32_u24 v7, v7, s6, v4
	s_waitcnt vmcnt(15)
	ds_write_b32 v7, v164 offset:0
	ds_write_b32 v7, v165 offset:8208
	ds_write_b32 v7, v166 offset:16416
	ds_write_b32 v7, v167 offset:24624
	s_waitcnt vmcnt(14)
	ds_write_b32 v7, v168 offset:512
	ds_write_b32 v7, v169 offset:8720
	ds_write_b32 v7, v170 offset:16928
	ds_write_b32 v7, v171 offset:25136
	s_waitcnt vmcnt(13)
	ds_write_b32 v7, v172 offset:1024
	ds_write_b32 v7, v173 offset:9232
	ds_write_b32 v7, v174 offset:17440
	ds_write_b32 v7, v175 offset:25648
	s_waitcnt vmcnt(12)
	ds_write_b32 v7, v176 offset:1536
	ds_write_b32 v7, v177 offset:9744
	ds_write_b32 v7, v178 offset:17952
	ds_write_b32 v7, v179 offset:26160
	s_waitcnt vmcnt(11)
	ds_write_b32 v7, v180 offset:2048
	ds_write_b32 v7, v181 offset:10256
	ds_write_b32 v7, v182 offset:18464
	ds_write_b32 v7, v183 offset:26672
	s_waitcnt vmcnt(10)
	ds_write_b32 v7, v184 offset:2560
	ds_write_b32 v7, v185 offset:10768
	ds_write_b32 v7, v186 offset:18976
	ds_write_b32 v7, v187 offset:27184
	s_waitcnt vmcnt(9)
	ds_write_b32 v7, v188 offset:3072
	ds_write_b32 v7, v189 offset:11280
	ds_write_b32 v7, v190 offset:19488
	ds_write_b32 v7, v191 offset:27696
	s_waitcnt vmcnt(8)
	ds_write_b32 v7, v192 offset:3584
	ds_write_b32 v7, v193 offset:11792
	ds_write_b32 v7, v194 offset:20000
	ds_write_b32 v7, v195 offset:28208
	s_waitcnt vmcnt(7)
	ds_write_b32 v7, v200 offset:4096
	ds_write_b32 v7, v201 offset:12304
	ds_write_b32 v7, v202 offset:20512
	ds_write_b32 v7, v203 offset:28720
	s_waitcnt vmcnt(6)
	ds_write_b32 v7, v204 offset:4608
	ds_write_b32 v7, v205 offset:12816
	ds_write_b32 v7, v206 offset:21024
	ds_write_b32 v7, v207 offset:29232
	s_waitcnt vmcnt(5)
	ds_write_b32 v7, v208 offset:5120
	ds_write_b32 v7, v209 offset:13328
	ds_write_b32 v7, v210 offset:21536
	ds_write_b32 v7, v211 offset:29744
	s_waitcnt vmcnt(4)
	ds_write_b32 v7, v212 offset:5632
	ds_write_b32 v7, v213 offset:13840
	ds_write_b32 v7, v214 offset:22048
	ds_write_b32 v7, v215 offset:30256
	s_waitcnt vmcnt(3)
	ds_write_b32 v7, v216 offset:6144
	ds_write_b32 v7, v217 offset:14352
	ds_write_b32 v7, v218 offset:22560
	ds_write_b32 v7, v219 offset:30768
	s_waitcnt vmcnt(2)
	ds_write_b32 v7, v220 offset:6656
	ds_write_b32 v7, v221 offset:14864
	ds_write_b32 v7, v222 offset:23072
	ds_write_b32 v7, v223 offset:31280
	s_waitcnt vmcnt(1)
	ds_write_b32 v7, v224 offset:7168
	ds_write_b32 v7, v225 offset:15376
	ds_write_b32 v7, v226 offset:23584
	ds_write_b32 v7, v227 offset:31792
	s_waitcnt vmcnt(0)
	ds_write_b32 v7, v228 offset:7680
	ds_write_b32 v7, v229 offset:15888
	ds_write_b32 v7, v230 offset:24096
	ds_write_b32 v7, v231 offset:32304
	s_or_b64 exec, exec, s[0:1]
	s_lshl_b32 s0, s94, 3
	s_add_i32 s19, s79, s0
	s_cmpk_lt_i32 s19, 0x4000
	s_cbranch_scc0 .LBB0_782
	s_add_u32 s4, s88, 0x2ff00000
	s_addc_u32 s5, s89, 0
	s_add_u32 s6, s88, 0x22600000
	s_addc_u32 s7, s89, 0
	s_add_u32 s8, s88, 0x200000
	v_lshlrev_b32_e32 v2, 2, v196
	s_addc_u32 s9, s89, 0
	v_lshl_or_b32 v2, s19, 11, v2
	s_add_u32 s10, s88, 0x1a600000
	v_or_b32_e32 v4, 0x100, v2
	v_or_b32_e32 v8, 0x300, v2
	v_or_b32_e32 v10, 0x400, v2
	v_or_b32_e32 v12, 0x500, v2
	s_addc_u32 s11, s89, 0
	v_lshlrev_b32_e32 v103, 4, v196
	v_ashrrev_i32_e32 v3, 31, v2
	v_ashrrev_i32_e32 v5, 31, v4
	v_or_b32_e32 v6, 0x200, v2
	v_ashrrev_i32_e32 v9, 31, v8
	v_ashrrev_i32_e32 v11, 31, v10
	v_ashrrev_i32_e32 v13, 31, v12
	v_or_b32_e32 v14, 0x600, v2
	v_or_b32_e32 v16, 0x700, v2
	v_or_b32_e32 v62, 0x1c00, v103
	v_or_b32_e32 v63, 0x1800, v103
	v_or_b32_e32 v64, 0x1400, v103
	v_or_b32_e32 v65, 0x1000, v103
	v_lshl_add_u64 v[90:91], v[2:3], 2, s[12:13]
	v_ashrrev_i32_e32 v7, 31, v6
	v_lshl_add_u64 v[92:93], v[10:11], 2, s[12:13]
	v_lshl_add_u64 v[94:95], v[12:13], 2, s[12:13]
	v_ashrrev_i32_e32 v15, 31, v14
	v_ashrrev_i32_e32 v17, 31, v16
	v_lshl_add_u64 v[96:97], v[8:9], 1, s[10:11]
	v_lshl_add_u64 v[122:123], v[4:5], 1, s[10:11]
	v_lshl_add_u64 v[104:105], v[14:15], 2, s[12:13]
	v_lshl_add_u64 v[108:109], v[16:17], 2, s[12:13]
	v_lshl_add_u64 v[110:111], v[16:17], 1, s[10:11]
	v_lshl_add_u64 v[112:113], v[14:15], 1, s[10:11]
	v_lshl_add_u64 v[114:115], v[12:13], 1, s[10:11]
	v_lshl_add_u64 v[118:119], v[10:11], 1, s[10:11]
	v_lshl_add_u64 v[120:121], v[6:7], 1, s[10:11]
	v_lshl_add_u64 v[124:125], v[2:3], 1, s[10:11]
	global_load_dwordx4 v[2:5], v62, s[48:49]
	global_load_dwordx4 v[6:9], v62, s[46:47]
	global_load_dwordx4 v[10:13], v63, s[48:49]
	global_load_dwordx4 v[14:17], v63, s[46:47]
	global_load_dwordx4 v[18:21], v64, s[48:49]
	global_load_dwordx4 v[22:25], v64, s[46:47]
	global_load_dwordx4 v[26:29], v65, s[48:49]
	global_load_dwordx4 v[30:33], v65, s[46:47]
	global_load_dwordx4 v[34:37], v103, s[48:49] offset:3072
	global_load_dwordx4 v[38:41], v103, s[46:47] offset:3072
	global_load_dwordx4 v[42:45], v103, s[48:49] offset:2048
	global_load_dwordx4 v[46:49], v103, s[46:47] offset:2048
	global_load_dwordx4 v[50:53], v103, s[48:49] offset:1024
	global_load_dwordx4 v[54:57], v103, s[46:47] offset:1024
	global_load_dwordx4 v[58:61], v103, s[48:49]
	global_load_dwordx4 v[62:65], v103, s[46:47]
	global_load_dwordx4 v[66:69], v[90:91], off nt
	global_load_dwordx4 v[70:73], v[90:91], off offset:1024 nt
	global_load_dwordx4 v[74:77], v[90:91], off offset:2048 nt
	global_load_dwordx4 v[78:81], v[90:91], off offset:3072 nt
	global_load_dwordx2 v[98:99], v[124:125], off nt
	global_load_dwordx2 v[100:101], v[122:123], off nt
	global_load_dwordx2 v[106:107], v[120:121], off nt
	global_load_dwordx2 v[116:117], v[96:97], off nt
	global_load_dwordx4 v[82:85], v[92:93], off nt
	global_load_dwordx4 v[86:89], v[94:95], off nt
	s_nop 0
	global_load_dwordx4 v[90:93], v[104:105], off nt
	global_load_dwordx4 v[94:97], v[108:109], off nt
	global_load_dwordx2 v[122:123], v[118:119], off nt
	global_load_dwordx2 v[128:129], v[114:115], off nt
	global_load_dwordx2 v[134:135], v[112:113], off nt
	global_load_dwordx2 v[140:141], v[110:111], off nt
	s_add_u32 s14, s88, 0x100000
	s_addc_u32 s15, s89, 0
	v_add_u32_e32 v102, 0, v102
	s_add_u32 s16, s88, 0x10000
	v_add_u32_e32 v111, 0x24100, v102
	v_mbcnt_lo_u32_b32 v102, -1, 0
	s_addc_u32 s17, s89, 0
	s_lshl_b32 s24, s92, 3
	s_lshl_b32 s25, s92, 7
	s_lshl_b32 s26, s92, 14
	s_movk_i32 s27, 0x5ff
	s_mov_b32 s18, 0x3f9837f0
	v_mov_b32_e32 v148, 0x3727c5ac
	s_mov_b32 s28, 0x800000
	s_mov_b32 s29, 0xc3e00000
	v_mov_b32_e32 v149, -1
	v_mbcnt_hi_u32_b32 v150, -1, v102
	v_mov_b32_e32 v151, 0x43e00000
	s_branch .LBB0_776

.LBB0_776:
	s_ashr_i32 s30, s19, 12
	s_mul_i32 s20, s30, 0x3000
	s_mov_b64 s[0:1], 0
	v_mov_b32_e32 v102, v1
	v_mov_b32_e32 v103, v111
	s_waitcnt lgkmcnt(0)
	s_barrier
	v_add_u32_e32 v232, s20, v1
	v_add_u32_e32 v232, 0x1200, v232
	v_lshlrev_b32_e32 v232, 2, v232
	v_mov_b32_e32 v234, v232
	global_load_dword v234, v234, s[16:17]
	v_add_u32_e32 v235, 0x2000, v232
	global_load_dword v235, v235, s[16:17]
	v_add_u32_e32 v236, 0x4000, v232
	global_load_dword v236, v236, s[16:17]
	v_add_u32_e32 v237, 0x800, v232
	global_load_dword v237, v237, s[16:17]
	v_add_u32_e32 v238, 0x2800, v232
	global_load_dword v238, v238, s[16:17]
	v_add_u32_e32 v239, 0x4800, v232
	global_load_dword v239, v239, s[16:17]
	v_add_u32_e32 v240, 0x1000, v232
	global_load_dword v240, v240, s[16:17]
	v_add_u32_e32 v241, 0x3000, v232
	global_load_dword v241, v241, s[16:17]
	v_add_u32_e32 v242, 0x5000, v232
	global_load_dword v242, v242, s[16:17]
	v_add_u32_e32 v243, 0x1800, v232
	global_load_dword v243, v243, s[16:17]
	v_add_u32_e32 v244, 0x3800, v232
	global_load_dword v244, v244, s[16:17]
	v_add_u32_e32 v245, 0x5800, v232
	global_load_dword v245, v245, s[16:17]
	v_add_u32_e32 v233, 0xffffc000, v111
	s_waitcnt vmcnt(0)
	ds_write_b32 v233, v234 offset:0
	ds_write_b32 v233, v235 offset:8192
	ds_write_b32 v233, v236 offset:16384
	ds_write_b32 v233, v237 offset:2048
	ds_write_b32 v233, v238 offset:10240
	ds_write_b32 v233, v239 offset:18432
	ds_write_b32 v233, v240 offset:4096
	ds_write_b32 v233, v241 offset:12288
	ds_write_b32 v233, v242 offset:20480
	ds_write_b32 v233, v243 offset:6144
	ds_write_b32 v233, v244 offset:14336
	ds_write_b32 v233, v245 offset:22528
	s_or_b64 exec, exec, s[0:1]
	s_lshl_b32 s0, s19, 11
	s_lshl_b32 s31, s19, 4
	s_or_b32 s33, s0, 0x700
	s_waitcnt lgkmcnt(0)
	s_barrier
	s_branch .LBB0_780
